# speedup vs baseline: 1.0062x; 1.0062x over previous
.Lbody:
	s_waitcnt lgkmcnt(0)
	v_mfma_f32_32x32x16_f16 v[80:95], v[176:179], v[144:147], v[112:127]
	s_waitcnt vmcnt(8)
	v_cmp_ne_u32_e64 s[20:21], 0, v224
	s_add_u32 s31, s23, 1
	s_and_b32 s31, s31, 31
	s_lshl_b32 s31, s31, 8
	s_add_u32 s26, s31, s22
	s_add_u32 s31, s23, 3
	s_and_b32 s31, s31, 31
	s_mul_i32 s31, s31, 0xc0000
	s_add_u32 s24, s31, s18
	s_add_u32 s31, s23, 2
	s_and_b32 s31, s31, 31
	s_mul_i32 s31, s31, 0xc0000
	s_add_u32 s25, s31, s19
	s_cmp_eq_u64 s[20:21], -1
	s_cselect_b32 s34, s37, s38
	ds_read_b128 v[176:179], v225 offset:4608
	buffer_load_dword v224, v230, s[8:11], s26 offen
	v_exp_f32_e32 v64, v64
	v_exp_f32_e32 v65, v65
	v_cvt_pk_f16_f32 v208, v208, v209
	v_cvt_pk_f16_f32 v209, v210, v211
	v_mfma_f32_32x32x16_f16 v[80:95], v[180:183], v[148:151], v[80:95]
	ds_read_b128 v[180:183], v225 offset:4640
	v_cvt_pk_f16_f32 v160, v64, v65
	v_add_f32_e32 v64, v64, v65
	v_cvt_pk_f16_f32 v212, v212, v213
	v_exp_f32_e32 v66, v66
	v_exp_f32_e32 v67, v67
	v_cvt_pk_f16_f32 v213, v214, v215
	v_mfma_f32_32x32x16_f16 v[80:95], v[184:187], v[152:155], v[80:95]
	ds_write_b64 v227, v[208:209] offset:18432
	ds_write_b64 v227, v[212:213] offset:23040
	ds_read_b128 v[184:187], v225 offset:4672
	v_cvt_pk_f16_f32 v161, v66, v67
	v_add_f32_e32 v66, v66, v67
	v_exp_f32_e32 v68, v68
	v_exp_f32_e32 v69, v69
	v_mfma_f32_32x32x16_f16 v[80:95], v[188:191], v[156:159], v[80:95]
	ds_read_b128 v[188:191], v225 offset:4704
	v_cvt_pk_f16_f32 v162, v68, v69
	v_add_f32_e32 v68, v68, v69
	v_add_f32_e32 v231, v64, v66
	v_exp_f32_e32 v70, v70
	v_exp_f32_e32 v71, v71
	v_mfma_f32_32x32x16_f16 v[32:47], v[192:195], v[168:171], v[32:47]
	ds_read_b128 v[192:195], v226 offset:0
	v_cvt_pk_f16_f32 v163, v70, v71
	v_add_f32_e32 v70, v70, v71
	v_add_f32_e32 v231, v231, v68
	v_exp_f32_e32 v72, v72
	v_exp_f32_e32 v73, v73
	v_mfma_f32_32x32x16_f16 v[48:63], v[196:199], v[168:171], v[48:63]
	ds_read_b128 v[196:199], v226 offset:4608
	v_cvt_pk_f16_f32 v164, v72, v73
	v_add_f32_e32 v72, v72, v73
	v_add_f32_e32 v231, v231, v70
	v_exp_f32_e32 v74, v74
	v_exp_f32_e32 v75, v75
	v_mfma_f32_32x32x16_f16 v[32:47], v[200:203], v[172:175], v[32:47]
	ds_read_b128 v[200:203], v226 offset:32
	v_cvt_pk_f16_f32 v165, v74, v75
	v_add_f32_e32 v74, v74, v75
	v_add_f32_e32 v231, v231, v72
	v_exp_f32_e32 v76, v76
	v_exp_f32_e32 v77, v77
	v_mfma_f32_32x32x16_f16 v[48:63], v[204:207], v[172:175], v[48:63]
	ds_read_b128 v[204:207], v226 offset:4640
	v_cvt_pk_f16_f32 v166, v76, v77
	v_add_f32_e32 v76, v76, v77
	v_add_f32_e32 v231, v231, v74
	v_exp_f32_e32 v78, v78
	v_exp_f32_e32 v79, v79
	v_add_f32_e32 v231, v231, v76
	v_cvt_pk_f16_f32 v167, v78, v79
	v_add_f32_e32 v78, v78, v79
	v_add_f32_e32 v231, v231, v78
	v_cmp_nge_f32_e32 vcc, s34, v231
	s_cbranch_vccnz .Lovf_a00
.Lovfret_a00:
	v_add_f32_e32 v232, v232, v231
	s_waitcnt lgkmcnt(4)
	v_mfma_f32_32x32x16_f16 v[64:79], v[176:179], v[128:131], v[96:111]
	v_exp_f32_e32 v80, v80
	v_exp_f32_e32 v81, v81
	v_mfma_f32_32x32x16_f16 v[64:79], v[180:183], v[132:135], v[64:79]
	buffer_load_dwordx4 v[208:211], v229, s[4:7], s24 offen
	v_cvt_pk_f16_f32 v168, v80, v81
	v_add_f32_e32 v80, v80, v81
	v_exp_f32_e32 v82, v82
	v_exp_f32_e32 v83, v83
	v_mfma_f32_32x32x16_f16 v[64:79], v[184:187], v[136:139], v[64:79]
	buffer_load_dwordx4 v[212:215], v252, s[4:7], s24 offen
	v_cvt_pk_f16_f32 v169, v82, v83
	v_add_f32_e32 v82, v82, v83
	v_exp_f32_e32 v84, v84
	v_exp_f32_e32 v85, v85
	v_mfma_f32_32x32x16_f16 v[64:79], v[188:191], v[140:143], v[64:79]
	v_cvt_pk_f16_f32 v170, v84, v85
	v_add_f32_e32 v84, v84, v85
	v_add_f32_e32 v231, v80, v82
	v_exp_f32_e32 v86, v86
	v_exp_f32_e32 v87, v87
	s_waitcnt lgkmcnt(0)
	v_mfma_f32_32x32x16_f16 v[0:15], v[192:195], v[160:163], v[0:15]
	v_cvt_pk_f16_f32 v171, v86, v87
	v_add_f32_e32 v86, v86, v87
	v_add_f32_e32 v231, v231, v84
	v_exp_f32_e32 v88, v88
	v_exp_f32_e32 v89, v89
	v_mfma_f32_32x32x16_f16 v[16:31], v[196:199], v[160:163], v[16:31]
	v_cvt_pk_f16_f32 v172, v88, v89
	v_add_f32_e32 v88, v88, v89
	v_add_f32_e32 v231, v231, v86
	v_exp_f32_e32 v90, v90
	v_exp_f32_e32 v91, v91
	v_mfma_f32_32x32x16_f16 v[0:15], v[200:203], v[164:167], v[0:15]
	v_cvt_pk_f16_f32 v173, v90, v91
	v_add_f32_e32 v90, v90, v91
	v_add_f32_e32 v231, v231, v88
	v_exp_f32_e32 v92, v92
	v_exp_f32_e32 v93, v93
	v_mfma_f32_32x32x16_f16 v[16:31], v[204:207], v[164:167], v[16:31]
	v_cvt_pk_f16_f32 v174, v92, v93
	v_add_f32_e32 v92, v92, v93
	v_add_f32_e32 v231, v231, v90
	v_exp_f32_e32 v94, v94
	v_exp_f32_e32 v95, v95
	v_add_f32_e32 v231, v231, v92
	v_cvt_pk_f16_f32 v175, v94, v95
	v_add_f32_e32 v94, v94, v95
	v_add_f32_e32 v231, v231, v94
	v_cmp_nge_f32_e32 vcc, s34, v231
	s_cbranch_vccnz .Lovf_b00
.Lovfret_b00:
	v_add_f32_e32 v233, v233, v231
	s_waitcnt lgkmcnt(0)
	v_mfma_f32_32x32x16_f16 v[80:95], v[176:179], v[144:147], v[112:127]
	ds_read_b128 v[176:179], v225 offset:9216
	s_waitcnt vmcnt(3)
	v_exp_f32_e32 v64, v64
	v_exp_f32_e32 v65, v65
	v_cvt_pk_f16_f32 v216, v216, v217
	v_cvt_pk_f16_f32 v217, v218, v219
	v_mfma_f32_32x32x16_f16 v[80:95], v[180:183], v[148:151], v[80:95]
	ds_read_b128 v[180:183], v225 offset:9248
	v_cvt_pk_f16_f32 v160, v64, v65
	v_add_f32_e32 v64, v64, v65
	v_cvt_pk_f16_f32 v218, v220, v221
	v_exp_f32_e32 v66, v66
	v_exp_f32_e32 v67, v67
	v_cvt_pk_f16_f32 v219, v222, v223
	v_mfma_f32_32x32x16_f16 v[80:95], v[184:187], v[152:155], v[80:95]
	ds_write_b128 v228, v[216:219] offset:9216
	ds_read_b128 v[184:187], v225 offset:9280
	v_cvt_pk_f16_f32 v161, v66, v67
	v_add_f32_e32 v66, v66, v67
	v_exp_f32_e32 v68, v68
	v_exp_f32_e32 v69, v69
	v_mfma_f32_32x32x16_f16 v[80:95], v[188:191], v[156:159], v[80:95]
	ds_read_b128 v[188:191], v225 offset:9312
	v_cvt_pk_f16_f32 v162, v68, v69
	v_add_f32_e32 v68, v68, v69
	v_add_f32_e32 v231, v64, v66
	v_exp_f32_e32 v70, v70
	v_exp_f32_e32 v71, v71
	v_mfma_f32_32x32x16_f16 v[32:47], v[192:195], v[168:171], v[32:47]
	ds_read_b128 v[192:195], v226 offset:64
	v_cvt_pk_f16_f32 v163, v70, v71
	v_add_f32_e32 v70, v70, v71
	v_add_f32_e32 v231, v231, v68
	v_exp_f32_e32 v72, v72
	v_exp_f32_e32 v73, v73
	v_mfma_f32_32x32x16_f16 v[48:63], v[196:199], v[168:171], v[48:63]
	ds_read_b128 v[196:199], v226 offset:4672
	v_cvt_pk_f16_f32 v164, v72, v73
	v_add_f32_e32 v72, v72, v73
	v_add_f32_e32 v231, v231, v70
	v_exp_f32_e32 v74, v74
	v_exp_f32_e32 v75, v75
	v_mfma_f32_32x32x16_f16 v[32:47], v[200:203], v[172:175], v[32:47]
	ds_read_b128 v[200:203], v226 offset:96
	v_cvt_pk_f16_f32 v165, v74, v75
	v_add_f32_e32 v74, v74, v75
	v_add_f32_e32 v231, v231, v72
	v_exp_f32_e32 v76, v76
	v_exp_f32_e32 v77, v77
	v_mfma_f32_32x32x16_f16 v[48:63], v[204:207], v[172:175], v[48:63]
	ds_read_b128 v[204:207], v226 offset:4704
	v_cvt_pk_f16_f32 v166, v76, v77
	v_add_f32_e32 v76, v76, v77
	v_add_f32_e32 v231, v231, v74
	v_exp_f32_e32 v78, v78
	v_exp_f32_e32 v79, v79
	v_add_f32_e32 v231, v231, v76
	v_cvt_pk_f16_f32 v167, v78, v79
	v_add_f32_e32 v78, v78, v79
	v_add_f32_e32 v231, v231, v78
	v_cmp_nge_f32_e32 vcc, s34, v231
	s_cbranch_vccnz .Lovf_a01
.Lovfret_a01:
	v_add_f32_e32 v232, v232, v231
	s_waitcnt lgkmcnt(4)
	v_mfma_f32_32x32x16_f16 v[64:79], v[176:179], v[128:131], v[96:111]
	buffer_load_dword v216, v230, s[4:7], s25 offen
	v_exp_f32_e32 v80, v80
	v_exp_f32_e32 v81, v81
	v_mfma_f32_32x32x16_f16 v[64:79], v[180:183], v[132:135], v[64:79]
	buffer_load_dword v217, v245, s[4:7], s25 offen
	v_cvt_pk_f16_f32 v168, v80, v81
	v_add_f32_e32 v80, v80, v81
	v_exp_f32_e32 v82, v82
	v_exp_f32_e32 v83, v83
	v_mfma_f32_32x32x16_f16 v[64:79], v[184:187], v[136:139], v[64:79]
	buffer_load_dword v218, v246, s[4:7], s25 offen
	v_cvt_pk_f16_f32 v169, v82, v83
	v_add_f32_e32 v82, v82, v83
	v_exp_f32_e32 v84, v84
	v_exp_f32_e32 v85, v85
	v_mfma_f32_32x32x16_f16 v[64:79], v[188:191], v[140:143], v[64:79]
	buffer_load_dword v219, v247, s[4:7], s25 offen
	v_cvt_pk_f16_f32 v170, v84, v85
	v_add_f32_e32 v84, v84, v85
	v_add_f32_e32 v231, v80, v82
	v_exp_f32_e32 v86, v86
	v_exp_f32_e32 v87, v87
	s_waitcnt lgkmcnt(0)
	v_mfma_f32_32x32x16_f16 v[0:15], v[192:195], v[160:163], v[0:15]
	buffer_load_dword v220, v248, s[4:7], s25 offen
	v_cvt_pk_f16_f32 v171, v86, v87
	v_add_f32_e32 v86, v86, v87
	v_add_f32_e32 v231, v231, v84
	v_exp_f32_e32 v88, v88
	v_exp_f32_e32 v89, v89
	v_mfma_f32_32x32x16_f16 v[16:31], v[196:199], v[160:163], v[16:31]
	buffer_load_dword v221, v249, s[4:7], s25 offen
	v_cvt_pk_f16_f32 v172, v88, v89
	v_add_f32_e32 v88, v88, v89
	v_add_f32_e32 v231, v231, v86
	v_exp_f32_e32 v90, v90
	v_exp_f32_e32 v91, v91
	v_mfma_f32_32x32x16_f16 v[0:15], v[200:203], v[164:167], v[0:15]
	buffer_load_dword v222, v250, s[4:7], s25 offen
	v_cvt_pk_f16_f32 v173, v90, v91
	v_add_f32_e32 v90, v90, v91
	v_add_f32_e32 v231, v231, v88
	v_exp_f32_e32 v92, v92
	v_exp_f32_e32 v93, v93
	v_mfma_f32_32x32x16_f16 v[16:31], v[204:207], v[164:167], v[16:31]
	buffer_load_dword v223, v251, s[4:7], s25 offen
	v_cvt_pk_f16_f32 v174, v92, v93
	v_add_f32_e32 v92, v92, v93
	v_add_f32_e32 v231, v231, v90
	v_exp_f32_e32 v94, v94
	v_exp_f32_e32 v95, v95
	v_add_f32_e32 v231, v231, v92
	v_cvt_pk_f16_f32 v175, v94, v95
	v_add_f32_e32 v94, v94, v95
	v_add_f32_e32 v231, v231, v94
	v_cmp_nge_f32_e32 vcc, s34, v231
	s_cbranch_vccnz .Lovf_b01
.Lovfret_b01:
	v_add_f32_e32 v233, v233, v231
	s_waitcnt lgkmcnt(6)
	s_barrier
	s_add_u32 s23, s23, 1
	s_waitcnt lgkmcnt(0)
	v_mfma_f32_32x32x16_f16 v[80:95], v[176:179], v[144:147], v[112:127]
	s_waitcnt vmcnt(8)
	v_cmp_ne_u32_e64 s[20:21], 0, v224
	s_add_u32 s31, s23, 1
	s_and_b32 s31, s31, 31
	s_lshl_b32 s31, s31, 8
	s_add_u32 s26, s31, s22
	s_add_u32 s31, s23, 3
	s_and_b32 s31, s31, 31
	s_mul_i32 s31, s31, 0xc0000
	s_add_u32 s24, s31, s18
	s_add_u32 s31, s23, 2
	s_and_b32 s31, s31, 31
	s_mul_i32 s31, s31, 0xc0000
	s_add_u32 s25, s31, s19
	s_cmp_eq_u64 s[20:21], -1
	s_cselect_b32 s34, s37, s38
	ds_read_b128 v[176:179], v225 offset:13824
	buffer_load_dword v224, v230, s[8:11], s26 offen
	v_exp_f32_e32 v64, v64
	v_exp_f32_e32 v65, v65
	v_cvt_pk_f16_f32 v208, v208, v209
	v_cvt_pk_f16_f32 v209, v210, v211
	v_mfma_f32_32x32x16_f16 v[80:95], v[180:183], v[148:151], v[80:95]
	ds_read_b128 v[180:183], v225 offset:13856
	v_cvt_pk_f16_f32 v160, v64, v65
	v_add_f32_e32 v64, v64, v65
	v_cvt_pk_f16_f32 v212, v212, v213
	v_exp_f32_e32 v66, v66
	v_exp_f32_e32 v67, v67
	v_cvt_pk_f16_f32 v213, v214, v215
	v_mfma_f32_32x32x16_f16 v[80:95], v[184:187], v[152:155], v[80:95]
	ds_write_b64 v227, v[208:209] offset:27648
	ds_write_b64 v227, v[212:213] offset:32256
	ds_read_b128 v[184:187], v225 offset:13888
	v_cvt_pk_f16_f32 v161, v66, v67
	v_add_f32_e32 v66, v66, v67
	v_exp_f32_e32 v68, v68
	v_exp_f32_e32 v69, v69
	v_mfma_f32_32x32x16_f16 v[80:95], v[188:191], v[156:159], v[80:95]
	ds_read_b128 v[188:191], v225 offset:13920
	v_cvt_pk_f16_f32 v162, v68, v69
	v_add_f32_e32 v68, v68, v69
	v_add_f32_e32 v231, v64, v66
	v_exp_f32_e32 v70, v70
	v_exp_f32_e32 v71, v71
	v_mfma_f32_32x32x16_f16 v[32:47], v[192:195], v[168:171], v[32:47]
	ds_read_b128 v[192:195], v226 offset:9216
	v_cvt_pk_f16_f32 v163, v70, v71
	v_add_f32_e32 v70, v70, v71
	v_add_f32_e32 v231, v231, v68
	v_exp_f32_e32 v72, v72
	v_exp_f32_e32 v73, v73
	v_mfma_f32_32x32x16_f16 v[48:63], v[196:199], v[168:171], v[48:63]
	ds_read_b128 v[196:199], v226 offset:13824
	v_cvt_pk_f16_f32 v164, v72, v73
	v_add_f32_e32 v72, v72, v73
	v_add_f32_e32 v231, v231, v70
	v_exp_f32_e32 v74, v74
	v_exp_f32_e32 v75, v75
	v_mfma_f32_32x32x16_f16 v[32:47], v[200:203], v[172:175], v[32:47]
	ds_read_b128 v[200:203], v226 offset:9248
	v_cvt_pk_f16_f32 v165, v74, v75
	v_add_f32_e32 v74, v74, v75
	v_add_f32_e32 v231, v231, v72
	v_exp_f32_e32 v76, v76
	v_exp_f32_e32 v77, v77
	v_mfma_f32_32x32x16_f16 v[48:63], v[204:207], v[172:175], v[48:63]
	ds_read_b128 v[204:207], v226 offset:13856
	v_cvt_pk_f16_f32 v166, v76, v77
	v_add_f32_e32 v76, v76, v77
	v_add_f32_e32 v231, v231, v74
	v_exp_f32_e32 v78, v78
	v_exp_f32_e32 v79, v79
	v_add_f32_e32 v231, v231, v76
	v_cvt_pk_f16_f32 v167, v78, v79
	v_add_f32_e32 v78, v78, v79
	v_add_f32_e32 v231, v231, v78
	v_cmp_nge_f32_e32 vcc, s34, v231
	s_cbranch_vccnz .Lovf_a10

.Lovfret_b10:
	v_add_f32_e32 v233, v233, v231
	s_waitcnt lgkmcnt(0)
	v_mfma_f32_32x32x16_f16 v[80:95], v[176:179], v[144:147], v[112:127]
	ds_read_b128 v[176:179], v225 offset:18432
	s_waitcnt vmcnt(3)
	v_exp_f32_e32 v64, v64
	v_exp_f32_e32 v65, v65
	v_cvt_pk_f16_f32 v216, v216, v217
	v_cvt_pk_f16_f32 v217, v218, v219
	v_mfma_f32_32x32x16_f16 v[80:95], v[180:183], v[148:151], v[80:95]
	ds_read_b128 v[180:183], v225 offset:18464
	v_cvt_pk_f16_f32 v160, v64, v65
	v_add_f32_e32 v64, v64, v65
	v_cvt_pk_f16_f32 v218, v220, v221
	v_exp_f32_e32 v66, v66
	v_exp_f32_e32 v67, v67
	v_cvt_pk_f16_f32 v219, v222, v223
	v_mfma_f32_32x32x16_f16 v[80:95], v[184:187], v[152:155], v[80:95]
	ds_write_b128 v228, v[216:219] offset:18432
	ds_read_b128 v[184:187], v225 offset:18496
	v_cvt_pk_f16_f32 v161, v66, v67
	v_add_f32_e32 v66, v66, v67
	v_exp_f32_e32 v68, v68
	v_exp_f32_e32 v69, v69
	v_mfma_f32_32x32x16_f16 v[80:95], v[188:191], v[156:159], v[80:95]
	ds_read_b128 v[188:191], v225 offset:18528
	v_cvt_pk_f16_f32 v162, v68, v69
	v_add_f32_e32 v68, v68, v69
	v_add_f32_e32 v231, v64, v66
	v_exp_f32_e32 v70, v70
	v_exp_f32_e32 v71, v71
	v_mfma_f32_32x32x16_f16 v[32:47], v[192:195], v[168:171], v[32:47]
	ds_read_b128 v[192:195], v226 offset:9280
	v_cvt_pk_f16_f32 v163, v70, v71
	v_add_f32_e32 v70, v70, v71
	v_add_f32_e32 v231, v231, v68
	v_exp_f32_e32 v72, v72
	v_exp_f32_e32 v73, v73
	v_mfma_f32_32x32x16_f16 v[48:63], v[196:199], v[168:171], v[48:63]
	ds_read_b128 v[196:199], v226 offset:13888
	v_cvt_pk_f16_f32 v164, v72, v73
	v_add_f32_e32 v72, v72, v73
	v_add_f32_e32 v231, v231, v70
	v_exp_f32_e32 v74, v74
	v_exp_f32_e32 v75, v75
	v_mfma_f32_32x32x16_f16 v[32:47], v[200:203], v[172:175], v[32:47]
	ds_read_b128 v[200:203], v226 offset:9312
	v_cvt_pk_f16_f32 v165, v74, v75
	v_add_f32_e32 v74, v74, v75
	v_add_f32_e32 v231, v231, v72
	v_exp_f32_e32 v76, v76
	v_exp_f32_e32 v77, v77
	v_mfma_f32_32x32x16_f16 v[48:63], v[204:207], v[172:175], v[48:63]
	ds_read_b128 v[204:207], v226 offset:13920
	v_cvt_pk_f16_f32 v166, v76, v77
	v_add_f32_e32 v76, v76, v77
	v_add_f32_e32 v231, v231, v74
	v_exp_f32_e32 v78, v78
	v_exp_f32_e32 v79, v79
	v_add_f32_e32 v231, v231, v76
	v_cvt_pk_f16_f32 v167, v78, v79
	v_add_f32_e32 v78, v78, v79
	v_add_f32_e32 v231, v231, v78
	v_cmp_nge_f32_e32 vcc, s34, v231
	s_cbranch_vccnz .Lovf_a11

.Lovfret_b11:
	v_add_f32_e32 v233, v233, v231
	s_waitcnt lgkmcnt(6)
	s_barrier
	s_add_u32 s23, s23, 1
	s_waitcnt lgkmcnt(0)
	v_mfma_f32_32x32x16_f16 v[80:95], v[176:179], v[144:147], v[112:127]
	s_waitcnt vmcnt(8)
	v_cmp_ne_u32_e64 s[20:21], 0, v224
	s_add_u32 s31, s23, 1
	s_and_b32 s31, s31, 31
	s_lshl_b32 s31, s31, 8
	s_add_u32 s26, s31, s22
	s_add_u32 s31, s23, 3
	s_and_b32 s31, s31, 31
	s_mul_i32 s31, s31, 0xc0000
	s_add_u32 s24, s31, s18
	s_add_u32 s31, s23, 2
	s_and_b32 s31, s31, 31
	s_mul_i32 s31, s31, 0xc0000
	s_add_u32 s25, s31, s19
	s_cmp_eq_u64 s[20:21], -1
	s_cselect_b32 s34, s37, s38
	ds_read_b128 v[176:179], v225 offset:23040
	buffer_load_dword v224, v230, s[8:11], s26 offen
	v_exp_f32_e32 v64, v64
	v_exp_f32_e32 v65, v65
	v_cvt_pk_f16_f32 v208, v208, v209
	v_cvt_pk_f16_f32 v209, v210, v211
	v_mfma_f32_32x32x16_f16 v[80:95], v[180:183], v[148:151], v[80:95]
	ds_read_b128 v[180:183], v225 offset:23072
	v_cvt_pk_f16_f32 v160, v64, v65
	v_add_f32_e32 v64, v64, v65
	v_cvt_pk_f16_f32 v212, v212, v213
	v_exp_f32_e32 v66, v66
	v_exp_f32_e32 v67, v67
	v_cvt_pk_f16_f32 v213, v214, v215
	v_mfma_f32_32x32x16_f16 v[80:95], v[184:187], v[152:155], v[80:95]
	ds_write_b64 v227, v[208:209] offset:0
	ds_write_b64 v227, v[212:213] offset:4608
	ds_read_b128 v[184:187], v225 offset:23104
	v_cvt_pk_f16_f32 v161, v66, v67
	v_add_f32_e32 v66, v66, v67
	v_exp_f32_e32 v68, v68
	v_exp_f32_e32 v69, v69
	v_mfma_f32_32x32x16_f16 v[80:95], v[188:191], v[156:159], v[80:95]
	ds_read_b128 v[188:191], v225 offset:23136
	v_cvt_pk_f16_f32 v162, v68, v69
	v_add_f32_e32 v68, v68, v69
	v_add_f32_e32 v231, v64, v66
	v_exp_f32_e32 v70, v70
	v_exp_f32_e32 v71, v71
	v_mfma_f32_32x32x16_f16 v[32:47], v[192:195], v[168:171], v[32:47]
	ds_read_b128 v[192:195], v226 offset:18432
	v_cvt_pk_f16_f32 v163, v70, v71
	v_add_f32_e32 v70, v70, v71
	v_add_f32_e32 v231, v231, v68
	v_exp_f32_e32 v72, v72
	v_exp_f32_e32 v73, v73
	v_mfma_f32_32x32x16_f16 v[48:63], v[196:199], v[168:171], v[48:63]
	ds_read_b128 v[196:199], v226 offset:23040
	v_cvt_pk_f16_f32 v164, v72, v73
	v_add_f32_e32 v72, v72, v73
	v_add_f32_e32 v231, v231, v70
	v_exp_f32_e32 v74, v74
	v_exp_f32_e32 v75, v75
	v_mfma_f32_32x32x16_f16 v[32:47], v[200:203], v[172:175], v[32:47]
	ds_read_b128 v[200:203], v226 offset:18464
	v_cvt_pk_f16_f32 v165, v74, v75
	v_add_f32_e32 v74, v74, v75
	v_add_f32_e32 v231, v231, v72
	v_exp_f32_e32 v76, v76
	v_exp_f32_e32 v77, v77
	v_mfma_f32_32x32x16_f16 v[48:63], v[204:207], v[172:175], v[48:63]
	ds_read_b128 v[204:207], v226 offset:23072
	v_cvt_pk_f16_f32 v166, v76, v77
	v_add_f32_e32 v76, v76, v77
	v_add_f32_e32 v231, v231, v74
	v_exp_f32_e32 v78, v78
	v_exp_f32_e32 v79, v79
	v_add_f32_e32 v231, v231, v76
	v_cvt_pk_f16_f32 v167, v78, v79
	v_add_f32_e32 v78, v78, v79
	v_add_f32_e32 v231, v231, v78
	v_cmp_nge_f32_e32 vcc, s34, v231
	s_cbranch_vccnz .Lovf_a20

.Lovfret_b20:
	v_add_f32_e32 v233, v233, v231
	s_waitcnt lgkmcnt(0)
	v_mfma_f32_32x32x16_f16 v[80:95], v[176:179], v[144:147], v[112:127]
	ds_read_b128 v[176:179], v225 offset:27648
	s_waitcnt vmcnt(3)
	v_exp_f32_e32 v64, v64
	v_exp_f32_e32 v65, v65
	v_cvt_pk_f16_f32 v216, v216, v217
	v_cvt_pk_f16_f32 v217, v218, v219
	v_mfma_f32_32x32x16_f16 v[80:95], v[180:183], v[148:151], v[80:95]
	ds_read_b128 v[180:183], v225 offset:27680
	v_cvt_pk_f16_f32 v160, v64, v65
	v_add_f32_e32 v64, v64, v65
	v_cvt_pk_f16_f32 v218, v220, v221
	v_exp_f32_e32 v66, v66
	v_exp_f32_e32 v67, v67
	v_cvt_pk_f16_f32 v219, v222, v223
	v_mfma_f32_32x32x16_f16 v[80:95], v[184:187], v[152:155], v[80:95]
	ds_write_b128 v228, v[216:219] offset:27648
	ds_read_b128 v[184:187], v225 offset:27712
	v_cvt_pk_f16_f32 v161, v66, v67
	v_add_f32_e32 v66, v66, v67
	v_exp_f32_e32 v68, v68
	v_exp_f32_e32 v69, v69
	v_mfma_f32_32x32x16_f16 v[80:95], v[188:191], v[156:159], v[80:95]
	ds_read_b128 v[188:191], v225 offset:27744
	v_cvt_pk_f16_f32 v162, v68, v69
	v_add_f32_e32 v68, v68, v69
	v_add_f32_e32 v231, v64, v66
	v_exp_f32_e32 v70, v70
	v_exp_f32_e32 v71, v71
	v_mfma_f32_32x32x16_f16 v[32:47], v[192:195], v[168:171], v[32:47]
	ds_read_b128 v[192:195], v226 offset:18496
	v_cvt_pk_f16_f32 v163, v70, v71
	v_add_f32_e32 v70, v70, v71
	v_add_f32_e32 v231, v231, v68
	v_exp_f32_e32 v72, v72
	v_exp_f32_e32 v73, v73
	v_mfma_f32_32x32x16_f16 v[48:63], v[196:199], v[168:171], v[48:63]
	ds_read_b128 v[196:199], v226 offset:23104
	v_cvt_pk_f16_f32 v164, v72, v73
	v_add_f32_e32 v72, v72, v73
	v_add_f32_e32 v231, v231, v70
	v_exp_f32_e32 v74, v74
	v_exp_f32_e32 v75, v75
	v_mfma_f32_32x32x16_f16 v[32:47], v[200:203], v[172:175], v[32:47]
	ds_read_b128 v[200:203], v226 offset:18528
	v_cvt_pk_f16_f32 v165, v74, v75
	v_add_f32_e32 v74, v74, v75
	v_add_f32_e32 v231, v231, v72
	v_exp_f32_e32 v76, v76
	v_exp_f32_e32 v77, v77
	v_mfma_f32_32x32x16_f16 v[48:63], v[204:207], v[172:175], v[48:63]
	ds_read_b128 v[204:207], v226 offset:23136
	v_cvt_pk_f16_f32 v166, v76, v77
	v_add_f32_e32 v76, v76, v77
	v_add_f32_e32 v231, v231, v74
	v_exp_f32_e32 v78, v78
	v_exp_f32_e32 v79, v79
	v_add_f32_e32 v231, v231, v76
	v_cvt_pk_f16_f32 v167, v78, v79
	v_add_f32_e32 v78, v78, v79
	v_add_f32_e32 v231, v231, v78
	v_cmp_nge_f32_e32 vcc, s34, v231
	s_cbranch_vccnz .Lovf_a21

.Lovfret_b21:
	v_add_f32_e32 v233, v233, v231
	s_waitcnt lgkmcnt(6)
	s_barrier
	s_add_u32 s23, s23, 1
	s_waitcnt lgkmcnt(0)
	v_mfma_f32_32x32x16_f16 v[80:95], v[176:179], v[144:147], v[112:127]
	s_waitcnt vmcnt(8)
	v_cmp_ne_u32_e64 s[20:21], 0, v224
	s_add_u32 s31, s23, 1
	s_and_b32 s31, s31, 31
	s_lshl_b32 s31, s31, 8
	s_add_u32 s26, s31, s22
	s_add_u32 s31, s23, 3
	s_and_b32 s31, s31, 31
	s_mul_i32 s31, s31, 0xc0000
	s_add_u32 s24, s31, s18
	s_add_u32 s31, s23, 2
	s_and_b32 s31, s31, 31
	s_mul_i32 s31, s31, 0xc0000
	s_add_u32 s25, s31, s19
	s_cmp_eq_u64 s[20:21], -1
	s_cselect_b32 s34, s37, s38
	ds_read_b128 v[176:179], v225 offset:32256
	buffer_load_dword v224, v230, s[8:11], s26 offen
	v_exp_f32_e32 v64, v64
	v_exp_f32_e32 v65, v65
	v_cvt_pk_f16_f32 v208, v208, v209
	v_cvt_pk_f16_f32 v209, v210, v211
	v_mfma_f32_32x32x16_f16 v[80:95], v[180:183], v[148:151], v[80:95]
	ds_read_b128 v[180:183], v225 offset:32288
	v_cvt_pk_f16_f32 v160, v64, v65
	v_add_f32_e32 v64, v64, v65
	v_cvt_pk_f16_f32 v212, v212, v213
	v_exp_f32_e32 v66, v66
	v_exp_f32_e32 v67, v67
	v_cvt_pk_f16_f32 v213, v214, v215
	v_mfma_f32_32x32x16_f16 v[80:95], v[184:187], v[152:155], v[80:95]
	ds_write_b64 v227, v[208:209] offset:9216
	ds_write_b64 v227, v[212:213] offset:13824
	ds_read_b128 v[184:187], v225 offset:32320
	v_cvt_pk_f16_f32 v161, v66, v67
	v_add_f32_e32 v66, v66, v67
	v_exp_f32_e32 v68, v68
	v_exp_f32_e32 v69, v69
	v_mfma_f32_32x32x16_f16 v[80:95], v[188:191], v[156:159], v[80:95]
	ds_read_b128 v[188:191], v225 offset:32352
	v_cvt_pk_f16_f32 v162, v68, v69
	v_add_f32_e32 v68, v68, v69
	v_add_f32_e32 v231, v64, v66
	v_exp_f32_e32 v70, v70
	v_exp_f32_e32 v71, v71
	v_mfma_f32_32x32x16_f16 v[32:47], v[192:195], v[168:171], v[32:47]
	ds_read_b128 v[192:195], v226 offset:27648
	v_cvt_pk_f16_f32 v163, v70, v71
	v_add_f32_e32 v70, v70, v71
	v_add_f32_e32 v231, v231, v68
	v_exp_f32_e32 v72, v72
	v_exp_f32_e32 v73, v73
	v_mfma_f32_32x32x16_f16 v[48:63], v[196:199], v[168:171], v[48:63]
	ds_read_b128 v[196:199], v226 offset:32256
	v_cvt_pk_f16_f32 v164, v72, v73
	v_add_f32_e32 v72, v72, v73
	v_add_f32_e32 v231, v231, v70
	v_exp_f32_e32 v74, v74
	v_exp_f32_e32 v75, v75
	v_mfma_f32_32x32x16_f16 v[32:47], v[200:203], v[172:175], v[32:47]
	ds_read_b128 v[200:203], v226 offset:27680
	v_cvt_pk_f16_f32 v165, v74, v75
	v_add_f32_e32 v74, v74, v75
	v_add_f32_e32 v231, v231, v72
	v_exp_f32_e32 v76, v76
	v_exp_f32_e32 v77, v77
	v_mfma_f32_32x32x16_f16 v[48:63], v[204:207], v[172:175], v[48:63]
	ds_read_b128 v[204:207], v226 offset:32288
	v_cvt_pk_f16_f32 v166, v76, v77
	v_add_f32_e32 v76, v76, v77
	v_add_f32_e32 v231, v231, v74
	v_exp_f32_e32 v78, v78
	v_exp_f32_e32 v79, v79
	v_add_f32_e32 v231, v231, v76
	v_cvt_pk_f16_f32 v167, v78, v79
	v_add_f32_e32 v78, v78, v79
	v_add_f32_e32 v231, v231, v78
	v_cmp_nge_f32_e32 vcc, s34, v231
	s_cbranch_vccnz .Lovf_a30

.Lovfret_b30:
	v_add_f32_e32 v233, v233, v231
	s_waitcnt lgkmcnt(0)
	v_mfma_f32_32x32x16_f16 v[80:95], v[176:179], v[144:147], v[112:127]
	ds_read_b128 v[176:179], v225 offset:0
	s_waitcnt vmcnt(3)
	v_exp_f32_e32 v64, v64
	v_exp_f32_e32 v65, v65
	v_cvt_pk_f16_f32 v216, v216, v217
	v_cvt_pk_f16_f32 v217, v218, v219
	v_mfma_f32_32x32x16_f16 v[80:95], v[180:183], v[148:151], v[80:95]
	ds_read_b128 v[180:183], v225 offset:32
	v_cvt_pk_f16_f32 v160, v64, v65
	v_add_f32_e32 v64, v64, v65
	v_cvt_pk_f16_f32 v218, v220, v221
	v_exp_f32_e32 v66, v66
	v_exp_f32_e32 v67, v67
	v_cvt_pk_f16_f32 v219, v222, v223
	v_mfma_f32_32x32x16_f16 v[80:95], v[184:187], v[152:155], v[80:95]
	ds_write_b128 v228, v[216:219] offset:0
	ds_read_b128 v[184:187], v225 offset:64
	v_cvt_pk_f16_f32 v161, v66, v67
	v_add_f32_e32 v66, v66, v67
	v_exp_f32_e32 v68, v68
	v_exp_f32_e32 v69, v69
	v_mfma_f32_32x32x16_f16 v[80:95], v[188:191], v[156:159], v[80:95]
	ds_read_b128 v[188:191], v225 offset:96
	v_cvt_pk_f16_f32 v162, v68, v69
	v_add_f32_e32 v68, v68, v69
	v_add_f32_e32 v231, v64, v66
	v_exp_f32_e32 v70, v70
	v_exp_f32_e32 v71, v71
	v_mfma_f32_32x32x16_f16 v[32:47], v[192:195], v[168:171], v[32:47]
	ds_read_b128 v[192:195], v226 offset:27712
	v_cvt_pk_f16_f32 v163, v70, v71
	v_add_f32_e32 v70, v70, v71
	v_add_f32_e32 v231, v231, v68
	v_exp_f32_e32 v72, v72
	v_exp_f32_e32 v73, v73
	v_mfma_f32_32x32x16_f16 v[48:63], v[196:199], v[168:171], v[48:63]
	ds_read_b128 v[196:199], v226 offset:32320
	v_cvt_pk_f16_f32 v164, v72, v73
	v_add_f32_e32 v72, v72, v73
	v_add_f32_e32 v231, v231, v70
	v_exp_f32_e32 v74, v74
	v_exp_f32_e32 v75, v75
	v_mfma_f32_32x32x16_f16 v[32:47], v[200:203], v[172:175], v[32:47]
	ds_read_b128 v[200:203], v226 offset:27744
	v_cvt_pk_f16_f32 v165, v74, v75
	v_add_f32_e32 v74, v74, v75
	v_add_f32_e32 v231, v231, v72
	v_exp_f32_e32 v76, v76
	v_exp_f32_e32 v77, v77
	v_mfma_f32_32x32x16_f16 v[48:63], v[204:207], v[172:175], v[48:63]
	ds_read_b128 v[204:207], v226 offset:32352
	v_cvt_pk_f16_f32 v166, v76, v77
	v_add_f32_e32 v76, v76, v77
	v_add_f32_e32 v231, v231, v74
	v_exp_f32_e32 v78, v78
	v_exp_f32_e32 v79, v79
	v_add_f32_e32 v231, v231, v76
	v_cvt_pk_f16_f32 v167, v78, v79
	v_add_f32_e32 v78, v78, v79
	v_add_f32_e32 v231, v231, v78
	v_cmp_nge_f32_e32 vcc, s34, v231
	s_cbranch_vccnz .Lovf_a31
